# V^T projection takes its tile list from workgroup index ^128: extra Q|K tile and extra V^T tile land on different workgroups
# speedup vs baseline: 1.0587x; 1.0013x over previous
.LBB0_323:
	v_readlane_b32 s0, v254, 35
	s_xor_b32 s0, s0, 0x80
	s_cmpk_gt_i32 s0, 0x21f
	v_mov_b32_e32 v130, 0x7f7f7f7f
	v_mbcnt_lo_u32_b32 v0, -1, 0
	v_mbcnt_hi_u32_b32 v0, -1, v0
	s_cbranch_scc1 .LBB0_339
	v_lshl_add_u32 v1, v0, 4, s23
	v_ashrrev_i32_e32 v2, 31, v1
	v_lshrrev_b32_e32 v2, 22, v2
	v_add_u32_e32 v2, v1, v2
	v_ashrrev_i32_e32 v2, 10, v2
	v_mul_i32_i24_e32 v3, 0x400, v2
	v_sub_u32_e32 v3, v1, v3
	s_waitcnt vmcnt(29)
	v_lshrrev_b32_e32 v4, 4, v3
	v_bitop3_b32 v3, v4, v3, 32 bitop3:0x6c
	v_ashrrev_i32_e32 v5, 31, v3
	v_lshrrev_b32_e32 v5, 26, v5
	v_lshlrev_b32_e32 v4, 3, v2
	v_add_u32_e32 v5, v3, v5
	v_and_b32_e32 v4, -16, v4
	s_waitcnt vmcnt(28)
	v_ashrrev_i32_e32 v6, 6, v5
	v_and_b32_e32 v5, 0xc0, v5
	v_add_u32_e32 v4, v6, v4
	v_sub_u32_e32 v3, v3, v5
	s_waitcnt vmcnt(27)
	v_mov_b32_e32 v8, 1
	v_lshlrev_b32_e32 v2, 5, v2
	v_ashrrev_i16_sdwa v3, v8, sext(v3) dst_sel:DWORD dst_unused:UNUSED_PAD src0_sel:DWORD src1_sel:BYTE_0
	v_lshlrev_b32_e32 v5, 1, v4
	v_lshrrev_b32_e32 v7, 2, v4
	v_and_b32_e32 v6, 3, v6
	s_mov_b32 s0, 0x3fffe0
	v_and_b32_e32 v2, 32, v2
	v_bfe_i32 v3, v3, 0, 16
	v_and_b32_e32 v5, 24, v5
	v_and_b32_e32 v7, 4, v7
	v_and_or_b32 v6, v4, s0, v6
	v_or3_b32 v5, v6, v7, v5
	v_add_lshl_u32 v2, v2, v3, 1
	v_add_u32_e32 v1, 0x2000, v1
	v_lshl_add_u32 v131, v4, 10, v2
	v_lshl_add_u32 v132, v5, 10, v2
	v_ashrrev_i32_e32 v2, 31, v1
	v_lshrrev_b32_e32 v2, 22, v2
	v_add_u32_e32 v2, v1, v2
	v_ashrrev_i32_e32 v2, 10, v2
	v_mul_i32_i24_e32 v3, 0x400, v2
	v_sub_u32_e32 v1, v1, v3
	v_lshrrev_b32_e32 v3, 4, v1
	v_bitop3_b32 v1, v3, v1, 32 bitop3:0x6c
	v_ashrrev_i32_e32 v4, 31, v1
	v_lshrrev_b32_e32 v4, 26, v4
	v_lshlrev_b32_e32 v3, 3, v2
	v_add_u32_e32 v4, v1, v4
	v_and_b32_e32 v3, -16, v3
	v_ashrrev_i32_e32 v5, 6, v4
	v_and_b32_e32 v4, 0xffc0, v4
	v_add_u32_e32 v3, v5, v3
	v_sub_u32_e32 v1, v1, v4
	v_and_b32_e32 v5, 3, v5
	v_lshrrev_b16_e32 v4, 7, v1
	v_and_or_b32 v5, v3, s0, v5
	s_add_u32 s18, s25, 0x200000
	v_readlane_b32 s0, v254, 35
	v_and_b32_e32 v4, 1, v4
	s_addc_u32 s19, s26, 0
	s_xor_b32 s0, s0, 0x80
	s_ashr_i32 s3, s0, 2
	s_lshl_b32 s0, s0, 8
	v_add_u16_e32 v1, v1, v4
	s_and_b32 s2, s0, 0x300
	v_lshlrev_b32_e32 v2, 5, v2
	v_ashrrev_i16_sdwa v1, v8, sext(v1) dst_sel:DWORD dst_unused:UNUSED_PAD src0_sel:DWORD src1_sel:BYTE_0
	v_lshlrev_b32_e32 v4, 1, v3
	v_lshrrev_b32_e32 v6, 2, v3
	s_lshl_b32 s36, s2, 10
	s_lshl_b32 s8, s3, 18
	v_and_b32_e32 v2, 32, v2
	v_bfe_i32 v1, v1, 0, 16
	v_and_b32_e32 v4, 24, v4
	v_and_b32_e32 v6, 4, v6
	s_add_u32 s0, s28, s8
	v_or3_b32 v4, v5, v6, v4
	v_add_lshl_u32 v1, v2, v1, 1
	s_addc_u32 s1, s29, 0
	s_or_b32 s4, s8, 0x20000
	s_mov_b32 m0, s35
	s_nop 4
	global_load_lds_dwordx4 v132, s[0:1]
	v_lshl_add_u32 v134, v4, 10, v1
	s_add_u32 s4, s28, s4
	s_mov_b32 m0, s38
	s_nop 4
	global_load_lds_dwordx4 v134, s[0:1]
	s_addc_u32 s5, s29, 0
	s_mov_b32 m0, s39
	s_nop 4
	global_load_lds_dwordx4 v132, s[4:5]
	s_add_u32 s6, s18, s36
	s_mov_b32 m0, s40
	s_nop 4
	global_load_lds_dwordx4 v134, s[4:5]
	s_addc_u32 s7, s19, 0
	s_mov_b32 m0, s30
	s_nop 4
	global_load_lds_dwordx4 v131, s[6:7]
	v_lshl_add_u32 v133, v3, 10, v1
	s_add_u32 s10, s6, 0x20000
	s_mov_b32 m0, s41
	s_nop 4
	global_load_lds_dwordx4 v133, s[6:7]
	s_addc_u32 s11, s7, 0
	s_mov_b32 m0, s42
	s_nop 4
	global_load_lds_dwordx4 v131, s[10:11]
	s_mov_b32 m0, s43
	s_nop 4
	global_load_lds_dwordx4 v133, s[10:11]
	v_cndmask_b32_e64 v1, 0, 1, s[16:17]
	v_cmp_ne_u32_e64 s[4:5], 1, v1
	s_andn2_b64 vcc, exec, s[16:17]
	s_cbranch_vccnz .LBB0_326
	s_barrier
.LBB0_326:
	s_lshl_b32 s9, s75, 12
	s_and_b32 s9, s9, 0x3000
	v_and_b32_e32 v1, 15, v0
	v_and_b32_e32 v2, 48, v0
	v_lshlrev_b32_e32 v0, 2, v0
	s_add_u32 s20, s76, 0x53c00000
	v_lshlrev_b32_e32 v1, 6, v1
	v_and_b32_e32 v0, 32, v0
	s_addc_u32 s21, s77, 0
	v_or_b32_e32 v3, v1, v2
	v_bitop3_b32 v1, v1, v0, v2 bitop3:0x36
	s_add_u32 s15, s15, 0x2000
	v_or_b32_e32 v135, s9, v1
	s_addc_u32 s24, s24, 0
	v_readlane_b32 s9, v254, 35
	s_xor_b32 s9, s9, 0x80
	s_lshl_b32 s11, s3, 8
	s_lshr_b32 s9, s9, 6
	s_add_i32 s10, s3, 0xffffff80
	s_and_b32 s11, s11, 0xf00
	s_cmpk_lt_i32 s3, 0x80
	s_cselect_b32 s3, s9, s10
	s_cselect_b32 s9, s11, 0x1000
	s_lshl_b32 s3, s3, 10
	s_or_b32 s3, s3, s2
	s_mulk_i32 s3, 0x1100
	s_or_b32 s3, s3, s9
	s_add_u32 s0, s0, 0x80
	s_addc_u32 s1, s1, 0
	s_waitcnt vmcnt(2)
	s_barrier
	s_mov_b32 m0, s44
	s_nop 4
	global_load_lds_dwordx4 v132, s[0:1]
	s_add_u32 s6, s6, 0x80
	s_mov_b32 m0, s45
	s_nop 4
	global_load_lds_dwordx4 v134, s[0:1]
	s_addc_u32 s7, s7, 0
	s_or_b32 s9, s8, 0x20080
	s_mov_b32 m0, s46
	s_nop 4
	global_load_lds_dwordx4 v131, s[6:7]
	s_add_u32 s10, s28, s9
	s_mov_b32 m0, s47
	s_nop 4
	global_load_lds_dwordx4 v133, s[6:7]
	s_addc_u32 s11, s29, 0
	s_and_b32 s9, s14, 64
	s_lshr_b32 s14, s14, 1
	s_mov_b32 m0, s48
	s_nop 4
	global_load_lds_dwordx4 v132, s[10:11]
	s_and_b32 s14, s14, 16
	s_mov_b32 m0, s49
	s_nop 4
	global_load_lds_dwordx4 v134, s[10:11]
	s_or_b32 s14, s14, s9
	s_waitcnt vmcnt(6)
	v_bitop3_b32 v128, v3, s22, v0 bitop3:0xde
	s_add_u32 s25, s18, 0x20080
	s_addc_u32 s26, s19, 0
	s_mov_b32 s27, 0
	v_add_u32_e32 v136, s91, v128
	s_mov_b32 s58, s8
	s_barrier
	v_mov_b32 v112, 0
	v_mov_b32 v113, 0
	v_mov_b32 v114, 0
	v_mov_b32 v115, 0
	v_mov_b32 v116, 0
	v_mov_b32 v117, 0
	v_mov_b32 v118, 0
	v_mov_b32 v119, 0
	v_mov_b32 v96, 0
	v_mov_b32 v97, 0
	v_mov_b32 v98, 0
	v_mov_b32 v99, 0
	v_mov_b32 v100, 0
	v_mov_b32 v101, 0
	v_mov_b32 v102, 0
	v_mov_b32 v103, 0
	v_mov_b32 v80, 0
	v_mov_b32 v81, 0
	v_mov_b32 v82, 0
	v_mov_b32 v83, 0
	v_mov_b32 v84, 0
	v_mov_b32 v85, 0
	v_mov_b32 v86, 0
	v_mov_b32 v87, 0
	s_waitcnt vmcnt(0)
	v_mov_b32 v56, 0
	v_mov_b32 v57, 0
	v_mov_b32 v58, 0
	v_mov_b32 v59, 0
	v_mov_b32 v60, 0
	v_mov_b32 v61, 0
	v_mov_b32 v62, 0
	v_mov_b32 v63, 0
	v_mov_b32 v120, 0
	v_mov_b32 v121, 0
	v_mov_b32 v122, 0
	v_mov_b32 v123, 0
	v_mov_b32 v124, 0
	v_mov_b32 v125, 0
	v_mov_b32 v126, 0
	v_mov_b32 v127, 0
	v_mov_b32 v104, 0
	v_mov_b32 v105, 0
	v_mov_b32 v106, 0
	v_mov_b32 v107, 0
	v_mov_b32 v108, 0
	v_mov_b32 v109, 0
	v_mov_b32 v110, 0
	v_mov_b32 v111, 0
	v_mov_b32 v88, 0
	v_mov_b32 v89, 0
	v_mov_b32 v90, 0
	v_mov_b32 v91, 0
	v_mov_b32 v92, 0
	v_mov_b32 v93, 0
	v_mov_b32 v94, 0
	v_mov_b32 v95, 0
	v_mov_b32 v72, 0
	v_mov_b32 v73, 0
	v_mov_b32 v74, 0
	v_mov_b32 v75, 0
	v_mov_b32 v76, 0
	v_mov_b32 v77, 0
	v_mov_b32 v78, 0
	v_mov_b32 v79, 0
	v_mov_b32 v48, 0
	v_mov_b32 v49, 0
	v_mov_b32 v50, 0
	v_mov_b32 v51, 0
	v_mov_b32 v52, 0
	v_mov_b32 v53, 0
	v_mov_b32 v54, 0
	v_mov_b32 v55, 0
	v_mov_b32 v32, 0
	v_mov_b32 v33, 0
	v_mov_b32 v34, 0
	v_mov_b32 v35, 0
	v_mov_b32 v36, 0
	v_mov_b32 v37, 0
	v_mov_b32 v38, 0
	v_mov_b32 v39, 0
	v_mov_b32 v16, 0
	v_mov_b32 v17, 0
	v_mov_b32 v18, 0
	v_mov_b32 v19, 0
	v_mov_b32 v20, 0
	v_mov_b32 v21, 0
	v_mov_b32 v22, 0
	v_mov_b32 v23, 0
	v_mov_b32 v0, 0
	v_mov_b32 v1, 0
	v_mov_b32 v2, 0
	v_mov_b32 v3, 0
	v_mov_b32 v4, 0
	v_mov_b32 v5, 0
	v_mov_b32 v6, 0
	v_mov_b32 v7, 0
	v_mov_b32 v64, 0
	v_mov_b32 v65, 0
	v_mov_b32 v66, 0
	v_mov_b32 v67, 0
	v_mov_b32 v68, 0
	v_mov_b32 v69, 0
	v_mov_b32 v70, 0
	v_mov_b32 v71, 0
	v_mov_b32 v40, 0
	v_mov_b32 v41, 0
	v_mov_b32 v42, 0
	v_mov_b32 v43, 0
	v_mov_b32 v44, 0
	v_mov_b32 v45, 0
	v_mov_b32 v46, 0
	v_mov_b32 v47, 0
	v_mov_b32 v24, 0
	v_mov_b32 v25, 0
	v_mov_b32 v26, 0
	v_mov_b32 v27, 0
	v_mov_b32 v28, 0
	v_mov_b32 v29, 0
	v_mov_b32 v30, 0
	v_mov_b32 v31, 0
	v_mov_b32 v8, 0
	v_mov_b32 v9, 0
	v_mov_b32 v10, 0
	v_mov_b32 v11, 0
	v_mov_b32 v12, 0
	v_mov_b32 v13, 0
	v_mov_b32 v14, 0
	v_mov_b32 v15, 0
	s_branch .LBB0_329

.LBB0_329:
	s_add_i32 s27, s27, 1
	v_readlane_b32 s6, v254, 34
	s_mul_i32 s0, s27, s57
	s_mul_hi_u32 s1, s27, s6
	s_add_i32 s1, s1, s0
	s_mul_i32 s0, s27, s6
	v_readlane_b32 s6, v254, 35
	s_xor_b32 s6, s6, 0x80
	s_add_u32 s0, s0, s6
	s_addc_u32 s1, s1, s34
	v_mov_b64_e32 v[128:129], 0x220
	v_cmp_lt_i64_e64 s[6:7], s[0:1], v[128:129]
	v_mov_b64_e32 v[128:129], 0x21f
	v_cmp_gt_i64_e32 vcc, s[0:1], v[128:129]
	v_mov_b32_e32 v199, 1.0
	s_mov_b32 s60, s36
	s_cbranch_vccnz .LBB0_331
	s_ashr_i32 s1, s0, 2
	s_lshl_b32 s11, s1, 8
	s_lshr_b32 s9, s0, 6
	s_add_i32 s10, s1, 0xffffff80
	s_and_b32 s11, s11, 0xf00
	s_cmpk_lt_i32 s1, 0x80
	s_cselect_b32 s9, s9, s10
	s_cselect_b32 s10, s11, 0x1000
	s_lshl_b32 s0, s0, 8
	s_and_b32 s33, s0, 0x300
	s_lshl_b32 s0, s9, 10
	s_or_b32 s0, s0, s33
	s_mulk_i32 s0, 0x1100
	s_lshl_b32 s60, s33, 10
	s_lshl_b32 s58, s1, 18
	s_or_b32 s59, s0, s10
